# speedup vs baseline: 1.0013x; 1.0013x over previous
_Z10ssim_finalPKfPf:
	s_load_dwordx4 s[4:7], s[0:1], 0x0
	v_lshlrev_b32_e32 v2, 4, v0
	v_mov_b32_e32 v3, 0
	s_waitcnt lgkmcnt(0)
	s_add_u32 s8, s4, 0x1000
	s_addc_u32 s9, s5, 0
	global_load_dwordx4 v[4:7], v2, s[4:5]
	global_load_dwordx4 v[8:11], v2, s[4:5] offset:1024
	global_load_dwordx4 v[12:15], v2, s[4:5] offset:2048
	global_load_dwordx4 v[16:19], v2, s[4:5] offset:3072
	global_load_dwordx4 v[20:23], v2, s[8:9]
	global_load_dwordx4 v[24:27], v2, s[8:9] offset:1024
	global_load_dwordx4 v[28:31], v2, s[8:9] offset:2048
	global_load_dwordx4 v[32:35], v2, s[8:9] offset:3072
	s_waitcnt vmcnt(7)
	v_cvt_f64_f32_e32 v[36:37], v4
	v_cvt_f64_f32_e32 v[38:39], v5
	v_cvt_f64_f32_e32 v[40:41], v6
	v_cvt_f64_f32_e32 v[42:43], v7
	v_add_f64 v[36:37], v[36:37], v[38:39]
	v_add_f64 v[40:41], v[40:41], v[42:43]
	v_add_f64 v[44:45], v[36:37], v[40:41]
	s_waitcnt vmcnt(6)
	v_cvt_f64_f32_e32 v[36:37], v8
	v_cvt_f64_f32_e32 v[38:39], v9
	v_cvt_f64_f32_e32 v[40:41], v10
	v_cvt_f64_f32_e32 v[42:43], v11
	v_add_f64 v[36:37], v[36:37], v[38:39]
	v_add_f64 v[40:41], v[40:41], v[42:43]
	v_add_f64 v[36:37], v[36:37], v[40:41]
	v_add_f64 v[44:45], v[44:45], v[36:37]
	s_waitcnt vmcnt(5)
	v_cvt_f64_f32_e32 v[36:37], v12
	v_cvt_f64_f32_e32 v[38:39], v13
	v_cvt_f64_f32_e32 v[40:41], v14
	v_cvt_f64_f32_e32 v[42:43], v15
	v_add_f64 v[36:37], v[36:37], v[38:39]
	v_add_f64 v[40:41], v[40:41], v[42:43]
	v_add_f64 v[36:37], v[36:37], v[40:41]
	v_add_f64 v[44:45], v[44:45], v[36:37]
	s_waitcnt vmcnt(4)
	v_cvt_f64_f32_e32 v[36:37], v16
	v_cvt_f64_f32_e32 v[38:39], v17
	v_cvt_f64_f32_e32 v[40:41], v18
	v_cvt_f64_f32_e32 v[42:43], v19
	v_add_f64 v[36:37], v[36:37], v[38:39]
	v_add_f64 v[40:41], v[40:41], v[42:43]
	v_add_f64 v[36:37], v[36:37], v[40:41]
	v_add_f64 v[44:45], v[44:45], v[36:37]
	s_waitcnt vmcnt(3)
	v_cvt_f64_f32_e32 v[36:37], v20
	v_cvt_f64_f32_e32 v[38:39], v21
	v_cvt_f64_f32_e32 v[40:41], v22
	v_cvt_f64_f32_e32 v[42:43], v23
	v_add_f64 v[36:37], v[36:37], v[38:39]
	v_add_f64 v[40:41], v[40:41], v[42:43]
	v_add_f64 v[36:37], v[36:37], v[40:41]
	v_add_f64 v[44:45], v[44:45], v[36:37]
	s_waitcnt vmcnt(2)
	v_cvt_f64_f32_e32 v[36:37], v24
	v_cvt_f64_f32_e32 v[38:39], v25
	v_cvt_f64_f32_e32 v[40:41], v26
	v_cvt_f64_f32_e32 v[42:43], v27
	v_add_f64 v[36:37], v[36:37], v[38:39]
	v_add_f64 v[40:41], v[40:41], v[42:43]
	v_add_f64 v[36:37], v[36:37], v[40:41]
	v_add_f64 v[44:45], v[44:45], v[36:37]
	s_waitcnt vmcnt(1)
	v_cvt_f64_f32_e32 v[36:37], v28
	v_cvt_f64_f32_e32 v[38:39], v29
	v_cvt_f64_f32_e32 v[40:41], v30
	v_cvt_f64_f32_e32 v[42:43], v31
	v_add_f64 v[36:37], v[36:37], v[38:39]
	v_add_f64 v[40:41], v[40:41], v[42:43]
	v_add_f64 v[36:37], v[36:37], v[40:41]
	v_add_f64 v[44:45], v[44:45], v[36:37]
	s_waitcnt vmcnt(0)
	v_cvt_f64_f32_e32 v[36:37], v32
	v_cvt_f64_f32_e32 v[38:39], v33
	v_cvt_f64_f32_e32 v[40:41], v34
	v_cvt_f64_f32_e32 v[42:43], v35
	v_add_f64 v[36:37], v[36:37], v[38:39]
	v_add_f64 v[40:41], v[40:41], v[42:43]
	v_add_f64 v[36:37], v[36:37], v[40:41]
	v_add_f64 v[44:45], v[44:45], v[36:37]
	s_nop 1
	v_mov_b32_dpp v46, v44 quad_perm:[1,0,3,2] row_mask:0xf bank_mask:0xf
	v_mov_b32_dpp v47, v45 quad_perm:[1,0,3,2] row_mask:0xf bank_mask:0xf
	v_add_f64 v[44:45], v[44:45], v[46:47]
	s_nop 1
	v_mov_b32_dpp v46, v44 quad_perm:[2,3,0,1] row_mask:0xf bank_mask:0xf
	v_mov_b32_dpp v47, v45 quad_perm:[2,3,0,1] row_mask:0xf bank_mask:0xf
	v_add_f64 v[44:45], v[44:45], v[46:47]
	s_nop 1
	v_mov_b32_dpp v46, v44 row_half_mirror row_mask:0xf bank_mask:0xf
	v_mov_b32_dpp v47, v45 row_half_mirror row_mask:0xf bank_mask:0xf
	v_add_f64 v[44:45], v[44:45], v[46:47]
	s_nop 1
	v_mov_b32_dpp v46, v44 row_mirror row_mask:0xf bank_mask:0xf
	v_mov_b32_dpp v47, v45 row_mirror row_mask:0xf bank_mask:0xf
	v_add_f64 v[44:45], v[44:45], v[46:47]
	s_nop 0
	v_readlane_b32 s10, v44, 0
	v_readlane_b32 s11, v45, 0
	v_readlane_b32 s12, v44, 16
	v_readlane_b32 s13, v45, 16
	v_readlane_b32 s14, v44, 32
	v_readlane_b32 s15, v45, 32
	v_readlane_b32 s16, v44, 48
	v_readlane_b32 s17, v45, 48
	v_cmp_eq_u32_e32 vcc, 0, v0
	s_and_saveexec_b64 s[2:3], vcc
	s_cbranch_execz .Lq_final_done
	v_mov_b32_e32 v0, s10
	v_mov_b32_e32 v1, s11
	v_add_f64 v[0:1], s[12:13], v[0:1]
	v_add_f64 v[0:1], s[14:15], v[0:1]
	v_add_f64 v[0:1], s[16:17], v[0:1]
	s_mov_b32 s2, 0
	s_mov_b32 s3, 0x415ec320
	v_div_scale_f64 v[4:5], s[8:9], s[2:3], s[2:3], v[0:1]
	v_rcp_f64_e32 v[6:7], v[4:5]
	s_nop 0
	v_fma_f64 v[8:9], -v[4:5], v[6:7], 1.0
	v_fmac_f64_e32 v[6:7], v[6:7], v[8:9]
	v_fma_f64 v[8:9], -v[4:5], v[6:7], 1.0
	v_fmac_f64_e32 v[6:7], v[6:7], v[8:9]
	v_div_scale_f64 v[8:9], vcc, v[0:1], s[2:3], v[0:1]
	v_mul_f64 v[10:11], v[8:9], v[6:7]
	v_fma_f64 v[4:5], -v[4:5], v[10:11], v[8:9]
	s_nop 1
	v_div_fmas_f64 v[4:5], v[4:5], v[6:7], v[10:11]
	v_div_fixup_f64 v[0:1], v[4:5], s[2:3], v[0:1]
	v_cvt_f32_f64_e32 v0, v[0:1]
	global_store_dword v3, v0, s[6:7] sc0 sc1
